# combined: padded 72-byte transpose tile + trimmed K/V DMA blocks + FFT read pipelining on the attention-embedded staging
# speedup vs baseline: 1.0186x; 1.0014x over previous
; #define LAS __attribute__((address_space(3)))
; #define WAIT_BAR(N) asm volatile("s_waitcnt vmcnt(" #N ") lgkmcnt(0)\n\ts_barrier" ::: "memory")
; #define DMA_K(t, slot) do { const bf16_t* sb_ = Kh + (long)(t) * KVBLK * DMK; glds16<0>(sb_, kvoff, (unsigned)__builtin_amdgcn_readfirstlane(kdst + (slot))); glds16<0>(sb_ + 64, kvoff, (unsigned)__builtin_amdgcn_readfirstlane(kdst + 8192 + (slot))); } while (0)
; template <int THRL> ...
;     ...
;   const bf16_t* Qw = Q + (size_t)(CTXL + qb * 128 + wq * QBLK) * DMK + head * 128 + comp * 64;
;   const bf16_t* Kh = K + head * 128; const bf16_t* Vh = V + head * 128;
;   const unsigned lds0 = (unsigned)(uintptr_t)shm;
;   LAS float* wsf = (LAS float*)(shm + LDS_WS) + wid * 64;
;   const unsigned kvoff = (unsigned)(lane * DMK + wid * 8) * 2u;
;   const unsigned vvoff = (unsigned)((16 * (wid & 3) + (lane >> 2)) * DMK + (wid >> 2) * 32 + (lane & 3) * 8) * 2u;
;   const unsigned kdst = lds0 + LDS_K + wid * 1024, vdst = lds0 + LDS_V + wid * 1024;
;     ...
;   const int vb0 = (int)(lds0 + LDS_V) + ((lane >> 4) & 1) * 32 + (lane & 3) * 8 + (4 * hi + ((lane & 15) >> 2)) * 64;
;   bf16x8 kf[8];
;   const lds_cptr shm3 = (lds_cptr)shm; const lds_cptr kp0 = shm3 + LDS_K + comp * 8192 + hi * 1024 + r32 * 16;
;   const lds_cptr vp0 = shm3 + LDS_V + ((lane >> 4) & 1) * 32 + (lane & 3) * 8 + (4 * hi + ((lane & 15) >> 2)) * 64;
;   DMA_K(0, 0); DMA_V(0, 0); DMA_K(1, SLOTB);
;   bf16x8 qr[4];
; #pragma unroll
;   for (int d0 = 0; d0 < 4; ++d0) qr[d0] = *reinterpret_cast<const bf16x8*>(&Qw[(long)r32 * DMK + d0 * 16 + hi * 8]);
;   float mhat = 0.f, l_reg = 0.f; f32x16 o[4]; o[0] = f32x16{}; o[1] = f32x16{}; o[2] = f32x16{}; o[3] = f32x16{}; f32x16 negm = f32x16{}; asm volatile("" : "+v"(negm));
;   bool resc = false;
;     ...
;   f32x16 pA0, pA1, pB0, pB1;
;   int sl_prev = 0, sl_cur = 0, sl_next = SLOTB;
;     ...
;   DMA_K(2, 2 * SLOTB);
;   WAIT_BAR(6);
;   qkt(pA0, pA1, kp0, qr, negm); asm volatile("s_nop 15\n\ts_nop 7" : "+v"(pA0), "+v"(pA1));
;   const lds_cptr qp = shm3 + LDS_Q + wid * 4096 + lane * 16;
; #pragma unroll
;   for (int d0 = 0; d0 < 4; ++d0) *(LAS bf16x8*)(shm + LDS_Q + wid * 4096 + lane * 16 + d0 * 1024) = qr[d0];
;   START(pA0, pA1);
; #pragma unroll
;   for (int r = 0; r < 16; ++r) pA1[r] = __builtin_amdgcn_exp2f(pA1[r]);
;   WAIT_BAR(0);
.LBB0_527:
	s_lshl_b32 s0, s28, 1
	s_and_b32 s0, s0, 0x700
	s_add_u32 s33, s26, s0
	s_addc_u32 s53, s27, 0
	s_bfe_u32 s41, s39, 0x20006
	s_lshl_b32 s0, s36, 4
	s_and_b32 s37, s0, 0xffffff80
	s_lshl_b32 s0, s41, 5
	s_or_b32 s0, s37, s0
	s_addk_i32 s0, 0x100
	s_ashr_i32 s1, s0, 31
	s_lshr_b32 s40, s39, 6
	s_lshr_b32 s42, s39, 8
	s_lshl_b64 s[0:1], s[0:1], 11
	s_add_u32 s0, s5, s0
	s_addc_u32 s1, s17, s1
	s_lshl_b32 s2, s36, 7
	s_and_b32 s14, s2, 0x380
	s_lshl_b32 s8, s14, 1
	s_add_u32 s0, s0, s8
	s_addc_u32 s1, s1, 0
	s_lshl_b32 s43, s42, 6
	s_lshl_b32 s2, s42, 7
	s_add_u32 s2, s0, s2
	s_addc_u32 s3, s1, 0
	s_add_u32 s20, s22, s8
	s_addc_u32 s21, s23, 0
	s_add_u32 s8, s24, s8
	s_addc_u32 s9, s25, 0
	s_lshl_b32 s0, s41, 15
	s_add_i32 s0, s0, s43
	v_add_u32_e32 v235, s0, v219
	s_lshl_b32 s0, s40, 10
	s_add_i32 s49, s0, 0
	s_and_b32 s1, s39, 0x3fffffc0
	s_lshl_b32 s38, s40, 4
	s_add_i32 s46, s49, 0xc000
	s_add_u32 s44, s20, 0x80
	v_add_u32_e32 v237, s38, v218
	s_mov_b32 s0, m0
	s_mov_b32 m0, s49
	s_nop 0
	global_load_lds_dwordx4 v237, s[20:21] offset:0
	s_mov_b32 m0, s0
	s_addc_u32 s45, s21, 0
	s_add_i32 s54, s49, 0x2000
	s_mov_b32 s0, m0
	s_mov_b32 m0, s54
	s_nop 0
	global_load_lds_dwordx4 v237, s[44:45] offset:0
	s_mov_b32 m0, s0
	s_add_u32 s50, s8, 0x80
	s_mov_b32 s0, m0
	s_mov_b32 m0, s46
	s_nop 0
	global_load_lds_dwordx4 v235, s[8:9] offset:0
	s_mov_b32 m0, s0
	s_addc_u32 s51, s9, 0
	s_add_i32 s45, s49, 0xe000
	s_mov_b32 s0, m0
	s_mov_b32 m0, s45
	s_nop 0
	global_load_lds_dwordx4 v235, s[50:51] offset:0
	s_mov_b32 m0, s0
	s_add_u32 s50, s20, 0x20000
	s_addc_u32 s51, s21, 0
	s_add_i32 s52, s49, 0x4000
	s_mov_b32 s0, m0
	s_mov_b32 m0, s52
	s_nop 0
	global_load_lds_dwordx4 v237, s[50:51] offset:0
	s_mov_b32 m0, s0
	s_add_u32 s56, s20, 0x20080
	s_addc_u32 s57, s21, 0
	s_add_i32 s51, s49, 0x6000
	s_mov_b32 s0, m0
	s_mov_b32 m0, s51
	s_nop 0
	global_load_lds_dwordx4 v237, s[56:57] offset:0
	s_mov_b32 m0, s0
	global_load_dwordx4 v[66:69], v229, s[2:3]
	global_load_dwordx4 v[70:73], v229, s[2:3] offset:32
	global_load_dwordx4 v[74:77], v229, s[2:3] offset:64
	global_load_dwordx4 v[78:81], v229, s[2:3] offset:96
	v_mov_b64_e32 v[48:49], v[32:33]
	s_add_u32 s2, s20, 0x40000
	v_mov_b64_e32 v[46:47], v[30:31]
	v_mov_b64_e32 v[44:45], v[28:29]
	v_mov_b64_e32 v[42:43], v[26:27]
	v_mov_b64_e32 v[40:41], v[24:25]
	v_mov_b64_e32 v[38:39], v[22:23]
	v_mov_b64_e32 v[36:37], v[20:21]
	v_mov_b64_e32 v[34:35], v[18:19]
	s_addc_u32 s3, s21, 0
	s_add_i32 s48, s49, 0x8000
	s_mov_b32 s0, m0
	s_mov_b32 m0, s48
	s_nop 0
	global_load_lds_dwordx4 v237, s[2:3] offset:0
	s_mov_b32 m0, s0
	s_add_u32 s2, s20, 0x40080
	s_addc_u32 s3, s21, 0
	s_add_i32 s47, s49, 0xa000
	s_mov_b32 s0, m0
	s_mov_b32 m0, s47
	s_nop 0
	global_load_lds_dwordx4 v237, s[2:3] offset:0
	s_mov_b32 m0, s0
	v_lshl_add_u32 v236, s42, 13, v221
	s_waitcnt vmcnt(6) lgkmcnt(0)
	s_barrier
	ds_read_b128 v[4:7], v236
	s_lshl_b32 s2, s40, 12
	v_add_u32_e32 v233, s2, v222
	s_lshl_b32 s1, s1, 2
	s_add_i32 s50, s1, 0
	s_add_i32 s50, s50, 0x18000
	s_add_u32 s2, s20, 0x60000
	s_addc_u32 s3, s21, 0
	v_mov_b32_e32 v3, v2
	v_mov_b32_e32 v12, v2
	v_mov_b32_e32 v13, v2
	s_movk_i32 s57, 0x4000
	s_mov_b32 s0, 0
	s_mov_b32 s55, 0x8000
	v_lshl_add_u32 v232, v217, 2, s50
	v_mov_b32_e32 v238, 0
	s_mov_b32 s56, -1
	s_waitcnt vmcnt(3) lgkmcnt(0)
	v_mfma_f32_32x32x16_bf16 v[50:65], v[4:7], v[66:69], v[34:49]
	ds_read_b128 v[4:7], v236 offset:512
	s_waitcnt lgkmcnt(0)
	v_mfma_f32_32x32x16_bf16 v[34:49], v[4:7], v[66:69], v[34:49]
	ds_read_b128 v[4:7], v236 offset:2048
	s_waitcnt vmcnt(2) lgkmcnt(0)
	v_mfma_f32_32x32x16_bf16 v[50:65], v[4:7], v[70:73], v[50:65]
	ds_read_b128 v[4:7], v236 offset:2560
	s_waitcnt lgkmcnt(0)
	v_mfma_f32_32x32x16_bf16 v[34:49], v[4:7], v[70:73], v[34:49]
	ds_read_b128 v[4:7], v236 offset:4096
	ds_read_b128 v[8:11], v236 offset:4608
	ds_read_b128 v[82:85], v236 offset:6656
	ds_read_b128 v[14:17], v236 offset:6144
	s_waitcnt vmcnt(1) lgkmcnt(3)
	v_mfma_f32_32x32x16_bf16 v[50:65], v[4:7], v[74:77], v[50:65]
	v_mov_b32_e32 v4, v2
	v_mov_b32_e32 v5, v2
	v_mov_b32_e32 v6, v2
	v_mov_b32_e32 v7, v2
	s_waitcnt lgkmcnt(2)
	v_mfma_f32_32x32x16_bf16 v[34:49], v[8:11], v[74:77], v[34:49]
	v_mov_b32_e32 v8, v2
	v_mov_b32_e32 v9, v2
	v_mov_b32_e32 v10, v2
	v_mov_b32_e32 v11, v2
	s_waitcnt vmcnt(0) lgkmcnt(0)
	v_mfma_f32_32x32x16_bf16 v[50:65], v[14:17], v[78:81], v[50:65]
	v_mov_b32_e32 v16, v2
	v_mov_b32_e32 v17, v2
	v_mov_b32_e32 v14, v2
	v_mov_b32_e32 v15, v2
	v_mfma_f32_32x32x16_bf16 v[34:49], v[82:85], v[78:81], v[34:49]
	s_nop 15
	s_nop 7
	ds_write_b128 v233, v[66:69]
	ds_write_b128 v233, v[70:73] offset:1024
	ds_write_b128 v233, v[74:77] offset:2048
	ds_write_b128 v233, v[78:81] offset:3072
	v_max3_f32 v66, v50, v51, v34
	v_max3_f32 v67, v52, v53, v35
	v_mov_b64_e32 v[96:97], v[16:17]
	v_max3_f32 v66, v66, v36, v37
	v_max3_f32 v67, v67, v56, v57
	v_mov_b64_e32 v[94:95], v[14:15]
	v_max3_f32 v66, v66, v54, v55
	v_max3_f32 v67, v67, v40, v41
	v_mov_b64_e32 v[92:93], v[12:13]
	v_max3_f32 v66, v66, v38, v39
	v_max3_f32 v67, v67, v60, v61
	v_mov_b64_e32 v[90:91], v[10:11]
	v_max3_f32 v66, v66, v58, v59
	v_max3_f32 v67, v67, v44, v45
	v_mov_b64_e32 v[88:89], v[8:9]
	v_max3_f32 v66, v66, v42, v43
	v_max3_f32 v67, v67, v64, v65
	v_mov_b64_e32 v[86:87], v[6:7]
	v_max3_f32 v66, v66, v62, v63
	v_max3_f32 v67, v67, v48, v49
	v_mov_b64_e32 v[84:85], v[4:5]
	v_max3_f32 v66, v66, v46, v47
	v_mov_b64_e32 v[82:83], v[2:3]
	v_max_f32_e32 v66, v66, v67
	s_nop 0
	v_mov_b32_e32 v67, v66
	s_nop 1
	v_permlane32_swap_b32_e32 v66, v67
	v_max_f32_e32 v66, v66, v67
	s_nop 0
	v_add_f32_e32 v234, v2, v66
	v_sub_f32_e32 v50, v50, v66
	v_sub_f32_e32 v34, v34, v66
	v_sub_f32_e32 v51, v51, v66
	v_sub_f32_e32 v35, v35, v66
	v_sub_f32_e32 v52, v52, v66
	s_nop 0
	v_xor_b32_e32 v98, 0x80000000, v234
	v_mov_b32_e32 v99, v98
	v_mov_b32_e32 v100, v98
	v_mov_b32_e32 v101, v98
	v_mov_b32_e32 v102, v98
	v_mov_b32_e32 v103, v98
	v_mov_b32_e32 v104, v98
	v_mov_b32_e32 v105, v98
	v_mov_b32_e32 v106, v98
	v_mov_b32_e32 v107, v98
	v_mov_b32_e32 v108, v98
	v_mov_b32_e32 v109, v98
	v_mov_b32_e32 v110, v98
	v_mov_b32_e32 v111, v98
	v_mov_b32_e32 v112, v98
	v_mov_b32_e32 v113, v98
	s_waitcnt vmcnt(0) lgkmcnt(0)
	s_barrier
; #define LAS __attribute__((address_space(3)))
; __device__ __forceinline__ unsigned pk2(float lo, float hi) { return f2bf(lo) | (f2bf(hi) << 16); }
; #define WAIT_BAR(N) asm volatile("s_waitcnt vmcnt(" #N ") lgkmcnt(0)\n\ts_barrier" ::: "memory")
; #define DMA_K(t, slot) do { const bf16_t* sb_ = Kh + (long)(t) * KVBLK * DMK; glds16<0>(sb_, kvoff, (unsigned)__builtin_amdgcn_readfirstlane(kdst + (slot))); glds16<0>(sb_ + 64, kvoff, (unsigned)__builtin_amdgcn_readfirstlane(kdst + 8192 + (slot))); } while (0)
; #define DMA_V(t, slot) do { const bf16_t* sb_ = Vh + (long)(t) * KVBLK * DMK; glds16<0>(sb_, vvoff, (unsigned)__builtin_amdgcn_readfirstlane(vdst + (slot))); glds16<0>(sb_ + 64, vvoff, (unsigned)__builtin_amdgcn_readfirstlane(vdst + 8192 + (slot))); } while (0)
; #define ROT() do { sl_prev = sl_cur; sl_cur = sl_next; sl_next = (sl_next == (NSLOT - 1) * SLOTB) ? 0 : sl_next + SLOTB; } while (0)
;     __device__ __forceinline__ const float* x() const { return (const float*)ld(0); }
;     __device__ __forceinline__ const float* c() const { return (const float*)ld(1); }
; template <int THRL> ...
;     ...
;   DMA_K(3, 0); DMA_V(1, SLOTB);
;   ROT();
;   kload8(kf, kp0 + sl_cur);
;   WAIT_BAR(4);
;   s16x4 vlo[4], vhi[4]; u32x4 pw0, pw1, pw2, pw3;
; template <bool NT = true> __device__ __forceinline__ void cvt_store(const CvtItem& d, const f32x4 (&v)[8], LAS float* scr, int lane) {
;     const int rr = lane >> 3, c4 = (lane & 7) * 4;
; #pragma unroll
;     for (int q = 0; q < 8; ++q) { LAS float* t = scr + (8 * q + rr) * 33 + c4; t[0] = v[q].x; t[1] = v[q].y; t[2] = v[q].z; t[3] = v[q].w; }
;     asm volatile("s_waitcnt lgkmcnt(0)" ::: "memory");
;     const int c = lane & 7;
; #pragma unroll
;     for (int j = 0; j < 4; ++j) { const int n = (lane >> 3) + 8 * j; const LAS float* s = scr + (8 * c) * 33 + n;
;         u32x4 o; o.x = pk2(s[0 * 33], s[1 * 33]); o.y = pk2(s[2 * 33], s[3 * 33]); o.z = pk2(s[4 * 33], s[5 * 33]); o.w = pk2(s[6 * 33], s[7 * 33]);
;         const int ng = d.n0 + n, drow = d.row_off + (d.ilv ? ((ng >> 7) * 256 + (ng & 127)) : ng);
;         if (NT) __builtin_nontemporal_store(o, (u32x4*)(d.dst + (size_t)drow * d.K + d.k0 + 8 * c)); else *(u32x4*)(d.dst + (size_t)drow * d.K + d.k0 + 8 * c) = o; }
	s_mov_b32 s1, m0
	s_mov_b32 m0, s49
	s_nop 0
	global_load_lds_dwordx4 v237, s[2:3] offset:0
	s_mov_b32 m0, s1
	s_add_u32 s2, s20, 0x60080
	s_addc_u32 s3, s21, 0
	s_mov_b32 s1, m0
	s_mov_b32 m0, s54
	s_nop 0
	global_load_lds_dwordx4 v237, s[2:3] offset:0
	s_mov_b32 m0, s1
	s_add_u32 s2, s8, 0x20000
	s_addc_u32 s3, s9, 0
	s_add_i32 s44, s49, 0x10000
	s_mov_b32 s1, m0
	s_mov_b32 m0, s44
	s_nop 0
	global_load_lds_dwordx4 v235, s[2:3] offset:0
	s_mov_b32 m0, s1
	s_add_u32 s2, s8, 0x20080
	s_addc_u32 s3, s9, 0
	s_add_i32 s43, s49, 0x12000
	s_mov_b32 s1, m0
	s_mov_b32 m0, s43
	s_nop 0
	global_load_lds_dwordx4 v235, s[2:3] offset:0
	s_mov_b32 m0, s1
	ds_read_b128 v[146:149], v236 offset:16384
	ds_read_b128 v[202:205], v236 offset:16896
	ds_read_b128 v[206:209], v236 offset:18432
	ds_read_b128 v[190:193], v236 offset:18944
	ds_read_b128 v[198:201], v236 offset:20480
	ds_read_b128 v[186:189], v236 offset:20992
	ds_read_b128 v[182:185], v236 offset:22528
	ds_read_b128 v[178:181], v236 offset:23040
	v_sub_f32_e32 v36, v36, v66
	v_sub_f32_e32 v53, v53, v66
	v_sub_f32_e32 v37, v37, v66
	v_sub_f32_e32 v54, v54, v66
	v_sub_f32_e32 v38, v38, v66
	v_sub_f32_e32 v55, v55, v66
	v_sub_f32_e32 v39, v39, v66
	v_sub_f32_e32 v56, v56, v66
	v_sub_f32_e32 v40, v40, v66
	v_sub_f32_e32 v57, v57, v66
	v_sub_f32_e32 v41, v41, v66
	v_sub_f32_e32 v58, v58, v66
	v_sub_f32_e32 v42, v42, v66
	v_sub_f32_e32 v59, v59, v66
	v_sub_f32_e32 v43, v43, v66
	v_sub_f32_e32 v60, v60, v66
	v_sub_f32_e32 v44, v44, v66
	v_sub_f32_e32 v61, v61, v66
	v_sub_f32_e32 v45, v45, v66
	v_sub_f32_e32 v62, v62, v66
	v_sub_f32_e32 v46, v46, v66
	v_sub_f32_e32 v63, v63, v66
	v_sub_f32_e32 v47, v47, v66
	v_sub_f32_e32 v64, v64, v66
	v_sub_f32_e32 v48, v48, v66
	v_sub_f32_e32 v65, v65, v66
	v_sub_f32_e32 v49, v49, v66
	v_exp_f32_e32 v130, v50
	v_exp_f32_e32 v131, v51
	v_exp_f32_e32 v132, v52
	v_exp_f32_e32 v133, v53
	v_exp_f32_e32 v134, v54
	v_exp_f32_e32 v135, v55
	v_exp_f32_e32 v136, v56
	v_exp_f32_e32 v137, v57
	v_exp_f32_e32 v138, v58
	v_exp_f32_e32 v139, v59
	v_exp_f32_e32 v140, v60
	v_exp_f32_e32 v141, v61
	v_exp_f32_e32 v142, v62
	v_exp_f32_e32 v143, v63
	v_exp_f32_e32 v144, v64
	v_exp_f32_e32 v145, v65
	v_exp_f32_e32 v114, v34
	v_exp_f32_e32 v115, v35
	v_exp_f32_e32 v116, v36
	v_exp_f32_e32 v117, v37
	v_exp_f32_e32 v118, v38
	v_exp_f32_e32 v119, v39
	v_exp_f32_e32 v120, v40
	v_exp_f32_e32 v121, v41
	v_exp_f32_e32 v122, v42
	v_exp_f32_e32 v123, v43
	v_exp_f32_e32 v124, v44
	v_exp_f32_e32 v125, v45
	v_exp_f32_e32 v126, v46
	v_exp_f32_e32 v127, v47
	v_exp_f32_e32 v128, v48
	v_exp_f32_e32 v129, v49
	s_waitcnt vmcnt(4) lgkmcnt(0)
	s_barrier
	v_mov_b64_e32 v[80:81], v[16:17]
	v_mov_b64_e32 v[48:49], v[16:17]
	v_mov_b64_e32 v[64:65], v[16:17]
	v_mov_b64_e32 v[78:79], v[14:15]
	v_mov_b64_e32 v[76:77], v[12:13]
	v_mov_b64_e32 v[74:75], v[10:11]
	v_mov_b64_e32 v[72:73], v[8:9]
	v_mov_b64_e32 v[70:71], v[6:7]
	v_mov_b64_e32 v[68:69], v[4:5]
	v_mov_b64_e32 v[66:67], v[2:3]
	v_mov_b64_e32 v[46:47], v[14:15]
	v_mov_b64_e32 v[44:45], v[12:13]
	v_mov_b64_e32 v[42:43], v[10:11]
	v_mov_b64_e32 v[40:41], v[8:9]
	v_mov_b64_e32 v[38:39], v[6:7]
	v_mov_b64_e32 v[36:37], v[4:5]
	v_mov_b64_e32 v[34:35], v[2:3]
	v_mov_b64_e32 v[62:63], v[14:15]
	v_mov_b64_e32 v[60:61], v[12:13]
	v_mov_b64_e32 v[58:59], v[10:11]
	v_mov_b64_e32 v[56:57], v[8:9]
	v_mov_b64_e32 v[54:55], v[6:7]
	v_mov_b64_e32 v[52:53], v[4:5]
	v_mov_b64_e32 v[50:51], v[2:3]
	v_mov_b32_e32 v244, 0x23ee8
	ds_read2_b64 v[250:253], v244 offset1:1
	ds_read_b64 v[254:255], v244 offset:16
	s_waitcnt lgkmcnt(0)
	v_readfirstlane_b32 s68, v250
	v_readfirstlane_b32 s69, v251
	v_readfirstlane_b32 s70, v252
	v_readfirstlane_b32 s71, v253
	v_readfirstlane_b32 s72, v254
	v_readfirstlane_b32 s73, v255
	ds_read_b64 v[250:251], v244 offset:40
	s_waitcnt lgkmcnt(0)
	v_readfirstlane_b32 s74, v250
	v_readfirstlane_b32 s75, v251
	s_add_u32 s76, s74, 0x16530000
	s_addc_u32 s77, s75, 0
	s_add_u32 s74, s74, 0xa530000
	s_addc_u32 s75, s75, 0
	v_lshrrev_b32_e32 v25, 3, v214
	v_and_b32_e32 v28, 7, v214
	v_lshlrev_b32_e32 v33, 4, v28
	v_lshl_add_u32 v24, v25, 12, v33
	v_lshl_add_u32 v246, v25, 13, v33
	v_mov_b32_e32 v29, 0x120
	v_mul_u32_u24_e32 v29, v29, v28
	v_lshl_add_u32 v29, v25, 1, v29
	s_mul_i32 s2, s40, 2304
	s_cmp_lt_u32 s40, 6
	s_mov_b32 s3, 0x20a00
	s_cselect_b32 s3, 0x20800, s3
	s_add_i32 s2, s2, s3
	v_add_u32_e32 v29, s2, v29
	v_add_u32_e32 v29, 32, v29
	v_mov_b32_e32 v32, 72
	v_mul_u32_u24_e32 v32, v32, v25
	v_lshl_add_u32 v32, v28, 3, v32
	v_add_u32_e32 v32, s2, v32
	s_mul_i32 s66, s96, 8
	s_add_i32 s66, s66, s40
	s_cmpk_lt_u32 s36, 0x100
	s_movk_i32 s67, 104
	s_cselect_b32 s67, 104, s67
	s_cselect_b32 s2, 0, 0x6800
	s_add_i32 s66, s66, s2
	s_add_i32 s90, s67, 6
	s_cmp_eq_u32 s67, 0
	s_cselect_b32 s90, -1, s90
	global_load_dword v249, v24, s[68:69]
	global_load_dword v249, v24, s[68:69]
	s_mov_b32 s32, m0
